# speedup vs baseline: 1.0641x; 1.0229x over previous
_Z13logits_kernelPKDv8_DF16bS1_PKfS3_PDv2_fS5_Pf:
	s_load_dwordx4 s[4:7], s[0:1], 0x0
	s_load_dwordx4 s[12:15], s[0:1], 0x10
	s_load_dwordx4 s[24:27], s[0:1], 0x20
	s_load_dwordx2 s[28:29], s[0:1], 0x30
	s_lshl_b32 s3, s2, 1
	s_and_b32 s3, s3, 14
	s_ashr_i32 s8, s2, 7
	s_bfe_u32 s10, s2, 0x40003
	s_add_i32 s3, s3, s8
	s_and_b32 s23, s2, 7
	v_lshrrev_b32_e32 v1, 6, v0
	v_and_b32_e32 v2, 63, v0
	s_movk_i32 s11, 0x3000
	v_add_u32_e32 v6, s23, v1
	v_lshlrev_b32_e32 v2, 4, v2
	v_and_b32_e32 v6, 3, v6
	v_and_b32_e32 v5, 31, v0
	v_mad_u32_u24 v6, v6, s11, v2
	v_lshlrev_b32_e32 v5, 2, v5
	s_mul_i32 s9, s23, 11
	s_lshr_b32 s9, s9, 5
	s_mul_i32 s9, s9, 3
	s_sub_i32 s23, s23, s9
	s_add_i32 s9, s23, 1
	s_cmp_ge_u32 s9, 3
	s_cselect_b32 s30, 0, s9
	s_add_i32 s9, s30, 1
	s_cmp_ge_u32 s9, 3
	s_cselect_b32 s31, 0, s9
	s_lshl_b32 s23, s23, 12
	s_lshl_b32 s30, s30, 12
	s_lshl_b32 s31, s31, 12
	s_lshl_b32 s9, s3, 9
	v_add_u32_e32 v2, s23, v6
	v_add_u32_e32 v3, s30, v6
	v_add_u32_e32 v4, s31, v6
	v_add_u32_e32 v5, s9, v5
	s_mul_i32 s8, s10, 0xc000
	s_mul_i32 s9, s3, 0x30000
	s_waitcnt lgkmcnt(0)
	s_load_dword s22, s[14:15], 0x0
	global_load_dword v248, v5, s[12:13]
	global_load_dword v249, v5, s[12:13] offset:128
	global_load_dword v250, v5, s[12:13] offset:256
	global_load_dword v251, v5, s[12:13] offset:384
	s_add_u32 s4, s4, s8
	s_addc_u32 s5, s5, 0
	s_add_u32 s6, s6, s9
	s_addc_u32 s7, s7, 0
	s_add_u32 s16, s6, 0xc000
	s_addc_u32 s17, s7, 0
	s_add_u32 s18, s6, 0x18000
	s_addc_u32 s19, s7, 0
	s_add_u32 s20, s6, 0x24000
	s_addc_u32 s21, s7, 0
	global_load_dwordx4 v[8:11], v2, s[4:5]
	global_load_dwordx4 v[56:59], v2, s[6:7]
	global_load_dwordx4 v[104:107], v2, s[16:17]
	global_load_dwordx4 v[152:155], v2, s[18:19]
	global_load_dwordx4 v[200:203], v2, s[20:21]
	global_load_dwordx4 v[12:15], v2, s[4:5] offset:1024
	global_load_dwordx4 v[60:63], v2, s[6:7] offset:1024
	global_load_dwordx4 v[108:111], v2, s[16:17] offset:1024
	global_load_dwordx4 v[156:159], v2, s[18:19] offset:1024
	global_load_dwordx4 v[204:207], v2, s[20:21] offset:1024
	global_load_dwordx4 v[16:19], v2, s[4:5] offset:2048
	global_load_dwordx4 v[64:67], v2, s[6:7] offset:2048
	global_load_dwordx4 v[112:115], v2, s[16:17] offset:2048
	global_load_dwordx4 v[160:163], v2, s[18:19] offset:2048
	global_load_dwordx4 v[208:211], v2, s[20:21] offset:2048
	global_load_dwordx4 v[20:23], v2, s[4:5] offset:3072
	global_load_dwordx4 v[68:71], v2, s[6:7] offset:3072
	global_load_dwordx4 v[116:119], v2, s[16:17] offset:3072
	global_load_dwordx4 v[164:167], v2, s[18:19] offset:3072
	global_load_dwordx4 v[212:215], v2, s[20:21] offset:3072
	global_load_dwordx4 v[24:27], v3, s[4:5]
	global_load_dwordx4 v[72:75], v3, s[6:7]
	global_load_dwordx4 v[120:123], v3, s[16:17]
	global_load_dwordx4 v[168:171], v3, s[18:19]
	global_load_dwordx4 v[216:219], v3, s[20:21]
	global_load_dwordx4 v[28:31], v3, s[4:5] offset:1024
	global_load_dwordx4 v[76:79], v3, s[6:7] offset:1024
	global_load_dwordx4 v[124:127], v3, s[16:17] offset:1024
	global_load_dwordx4 v[172:175], v3, s[18:19] offset:1024
	global_load_dwordx4 v[220:223], v3, s[20:21] offset:1024
	global_load_dwordx4 v[32:35], v3, s[4:5] offset:2048
	global_load_dwordx4 v[80:83], v3, s[6:7] offset:2048
	global_load_dwordx4 v[128:131], v3, s[16:17] offset:2048
	global_load_dwordx4 v[176:179], v3, s[18:19] offset:2048
	global_load_dwordx4 v[224:227], v3, s[20:21] offset:2048
	global_load_dwordx4 v[36:39], v3, s[4:5] offset:3072
	global_load_dwordx4 v[84:87], v3, s[6:7] offset:3072
	global_load_dwordx4 v[132:135], v3, s[16:17] offset:3072
	global_load_dwordx4 v[180:183], v3, s[18:19] offset:3072
	global_load_dwordx4 v[228:231], v3, s[20:21] offset:3072
	global_load_dwordx4 v[40:43], v4, s[4:5]
	global_load_dwordx4 v[88:91], v4, s[6:7]
	global_load_dwordx4 v[136:139], v4, s[16:17]
	global_load_dwordx4 v[184:187], v4, s[18:19]
	global_load_dwordx4 v[232:235], v4, s[20:21]
	global_load_dwordx4 v[44:47], v4, s[4:5] offset:1024
	global_load_dwordx4 v[92:95], v4, s[6:7] offset:1024
	global_load_dwordx4 v[140:143], v4, s[16:17] offset:1024
	global_load_dwordx4 v[188:191], v4, s[18:19] offset:1024
	global_load_dwordx4 v[236:239], v4, s[20:21] offset:1024
	global_load_dwordx4 v[48:51], v4, s[4:5] offset:2048
	global_load_dwordx4 v[96:99], v4, s[6:7] offset:2048
	global_load_dwordx4 v[144:147], v4, s[16:17] offset:2048
	global_load_dwordx4 v[192:195], v4, s[18:19] offset:2048
	global_load_dwordx4 v[240:243], v4, s[20:21] offset:2048
	global_load_dwordx4 v[52:55], v4, s[4:5] offset:3072
	global_load_dwordx4 v[100:103], v4, s[6:7] offset:3072
	global_load_dwordx4 v[148:151], v4, s[16:17] offset:3072
	global_load_dwordx4 v[196:199], v4, s[18:19] offset:3072
	global_load_dwordx4 v[244:247], v4, s[20:21] offset:3072
	s_waitcnt vmcnt(58)
	v_mfma_f32_32x32x16_bf16 a[0:15], v[8:11], v[56:59], 0
	s_waitcnt vmcnt(57)
	v_mfma_f32_32x32x16_bf16 a[0:15], v[8:11], v[104:107], a[0:15]
	s_waitcnt vmcnt(56)
	v_mfma_f32_32x32x16_bf16 a[0:15], v[8:11], v[152:155], a[0:15]
	s_waitcnt vmcnt(55)
	v_mfma_f32_32x32x16_bf16 a[0:15], v[8:11], v[200:203], a[0:15]
	s_waitcnt vmcnt(53)
	v_mfma_f32_32x32x16_bf16 a[0:15], v[12:15], v[60:63], a[0:15]
	s_waitcnt vmcnt(52)
	v_mfma_f32_32x32x16_bf16 a[0:15], v[12:15], v[108:111], a[0:15]
	s_waitcnt vmcnt(51)
	v_mfma_f32_32x32x16_bf16 a[0:15], v[12:15], v[156:159], a[0:15]
	s_waitcnt vmcnt(50)
	v_mfma_f32_32x32x16_bf16 a[0:15], v[12:15], v[204:207], a[0:15]
	s_waitcnt vmcnt(48)
	v_mfma_f32_32x32x16_bf16 a[0:15], v[16:19], v[64:67], a[0:15]
	s_waitcnt vmcnt(47)
	v_mfma_f32_32x32x16_bf16 a[0:15], v[16:19], v[112:115], a[0:15]
	s_waitcnt vmcnt(46)
	v_mfma_f32_32x32x16_bf16 a[0:15], v[16:19], v[160:163], a[0:15]
	s_waitcnt vmcnt(45)
	v_mfma_f32_32x32x16_bf16 a[0:15], v[16:19], v[208:211], a[0:15]
	s_waitcnt vmcnt(43)
	v_mfma_f32_32x32x16_bf16 a[0:15], v[20:23], v[68:71], a[0:15]
	s_waitcnt vmcnt(42)
	v_mfma_f32_32x32x16_bf16 a[0:15], v[20:23], v[116:119], a[0:15]
	s_waitcnt vmcnt(41)
	v_mfma_f32_32x32x16_bf16 a[0:15], v[20:23], v[164:167], a[0:15]
	s_waitcnt vmcnt(40)
	v_mfma_f32_32x32x16_bf16 a[0:15], v[20:23], v[212:215], a[0:15]
	s_waitcnt vmcnt(38)
	v_mfma_f32_32x32x16_bf16 a[0:15], v[24:27], v[72:75], a[0:15]
	s_waitcnt vmcnt(37)
	v_mfma_f32_32x32x16_bf16 a[0:15], v[24:27], v[120:123], a[0:15]
	s_waitcnt vmcnt(36)
	v_mfma_f32_32x32x16_bf16 a[0:15], v[24:27], v[168:171], a[0:15]
	s_waitcnt vmcnt(35)
	v_mfma_f32_32x32x16_bf16 a[0:15], v[24:27], v[216:219], a[0:15]
	s_waitcnt vmcnt(33)
	v_mfma_f32_32x32x16_bf16 a[0:15], v[28:31], v[76:79], a[0:15]
	s_waitcnt vmcnt(32)
	v_mfma_f32_32x32x16_bf16 a[0:15], v[28:31], v[124:127], a[0:15]
	s_waitcnt vmcnt(31)
	v_mfma_f32_32x32x16_bf16 a[0:15], v[28:31], v[172:175], a[0:15]
	s_waitcnt vmcnt(30)
	v_mfma_f32_32x32x16_bf16 a[0:15], v[28:31], v[220:223], a[0:15]
	s_waitcnt vmcnt(28)
	v_mfma_f32_32x32x16_bf16 a[0:15], v[32:35], v[80:83], a[0:15]
	s_waitcnt vmcnt(27)
	v_mfma_f32_32x32x16_bf16 a[0:15], v[32:35], v[128:131], a[0:15]
	s_waitcnt vmcnt(26)
	v_mfma_f32_32x32x16_bf16 a[0:15], v[32:35], v[176:179], a[0:15]
	s_waitcnt vmcnt(25)
	v_mfma_f32_32x32x16_bf16 a[0:15], v[32:35], v[224:227], a[0:15]
	s_waitcnt vmcnt(23)
	v_mfma_f32_32x32x16_bf16 a[0:15], v[36:39], v[84:87], a[0:15]
	s_waitcnt vmcnt(22)
	v_mfma_f32_32x32x16_bf16 a[0:15], v[36:39], v[132:135], a[0:15]
	s_waitcnt vmcnt(21)
	v_mfma_f32_32x32x16_bf16 a[0:15], v[36:39], v[180:183], a[0:15]
	s_waitcnt vmcnt(20)
	v_mfma_f32_32x32x16_bf16 a[0:15], v[36:39], v[228:231], a[0:15]
	s_waitcnt vmcnt(18)
	v_mfma_f32_32x32x16_bf16 a[0:15], v[40:43], v[88:91], a[0:15]
	s_waitcnt vmcnt(17)
	v_mfma_f32_32x32x16_bf16 a[0:15], v[40:43], v[136:139], a[0:15]
	s_waitcnt vmcnt(16)
	v_mfma_f32_32x32x16_bf16 a[0:15], v[40:43], v[184:187], a[0:15]
	s_waitcnt vmcnt(15)
	v_mfma_f32_32x32x16_bf16 a[0:15], v[40:43], v[232:235], a[0:15]
	s_waitcnt vmcnt(13)
	v_mfma_f32_32x32x16_bf16 a[0:15], v[44:47], v[92:95], a[0:15]
	s_waitcnt vmcnt(12)
	v_mfma_f32_32x32x16_bf16 a[0:15], v[44:47], v[140:143], a[0:15]
	s_waitcnt vmcnt(11)
	v_mfma_f32_32x32x16_bf16 a[0:15], v[44:47], v[188:191], a[0:15]
	s_waitcnt vmcnt(10)
	v_mfma_f32_32x32x16_bf16 a[0:15], v[44:47], v[236:239], a[0:15]
	v_add_f32_e32 v8, 0, v248
	v_add_f32_e32 v8, v8, v249
	v_add_f32_e32 v8, v8, v250
	v_add_f32_e32 v8, v8, v251
	v_mov_b32_e32 v9, 0x3fb8aa3b
	s_waitcnt lgkmcnt(0)
	v_mul_f32_e32 v9, s22, v9
	v_exp_f32_e32 v9, v9
	v_add_f32_e32 v10, 0x2b8cbccc, v8
	v_div_scale_f32 v11, s[8:9], v10, v10, v9
	v_rcp_f32_e32 v12, v11
	v_div_scale_f32 v13, vcc, v9, v10, v9
	v_fma_f32 v14, -v11, v12, 1.0
	v_fmac_f32_e32 v12, v14, v12
	v_mul_f32_e32 v14, v13, v12
	v_fma_f32 v15, -v11, v14, v13
	v_fmac_f32_e32 v14, v15, v12
	v_fma_f32 v11, -v11, v14, v13
	v_div_fmas_f32 v11, v11, v12, v14
	v_div_fixup_f32 v9, v11, v10, v9
	v_lshlrev_b32_e32 v10, 2, v0
	v_add_u32_e32 v10, 0x4000, v10
	v_cmp_gt_u32_e32 vcc, 32, v0
	s_and_saveexec_b64 s[8:9], vcc
	ds_write2_b32 v10, v8, v9 offset0:128 offset1:160
	s_mov_b64 exec, s[8:9]
	s_waitcnt vmcnt(8)
	v_mfma_f32_32x32x16_bf16 a[0:15], v[48:51], v[96:99], a[0:15]
	s_waitcnt vmcnt(7)
	v_mfma_f32_32x32x16_bf16 a[0:15], v[48:51], v[144:147], a[0:15]
	s_waitcnt vmcnt(6)
	v_mfma_f32_32x32x16_bf16 a[0:15], v[48:51], v[192:195], a[0:15]
	s_waitcnt vmcnt(5)
	v_mfma_f32_32x32x16_bf16 a[0:15], v[48:51], v[240:243], a[0:15]
	v_mul_u32_u24_e32 v1, 0x1080, v1
	s_movk_i32 s4, 0x7f
	s_movk_i32 s6, 0x84
	v_cmp_lt_u32_e32 vcc, s4, v0
	v_lshrrev_b32_e32 v11, 3, v0
	v_and_b32_e32 v10, 31, v0
	v_and_b32_e32 v11, 4, v11
	v_mul_u32_u24_e32 v11, 0x84, v11
	v_lshlrev_b32_e32 v9, 2, v10
	v_bfe_u32 v6, v0, 2, 5
	v_and_b32_e32 v7, 3, v0
	v_add3_u32 v1, v1, v11, v9
	v_lshlrev_b32_e32 v8, 3, v7
	s_waitcnt vmcnt(3)
	v_mfma_f32_32x32x16_bf16 a[0:15], v[52:55], v[100:103], a[0:15]
	s_waitcnt vmcnt(2)
	v_mfma_f32_32x32x16_bf16 a[0:15], v[52:55], v[148:151], a[0:15]
	s_waitcnt vmcnt(1)
	v_mfma_f32_32x32x16_bf16 a[0:15], v[52:55], v[196:199], a[0:15]
	s_waitcnt vmcnt(0)
	v_mfma_f32_32x32x16_bf16 a[0:15], v[52:55], v[244:247], a[0:15]
	s_nop 11
	ds_write_b32 v1, a0
	ds_write_b32 v1, a1 offset:132
	ds_write_b32 v1, a2 offset:264
	ds_write_b32 v1, a3 offset:396
	ds_write_b32 v1, a4 offset:1056
	ds_write_b32 v1, a5 offset:1188
	ds_write_b32 v1, a6 offset:1320
	ds_write_b32 v1, a7 offset:1452
	ds_write_b32 v1, a8 offset:2112
	ds_write_b32 v1, a9 offset:2244
	ds_write_b32 v1, a10 offset:2376
	ds_write_b32 v1, a11 offset:2508
	ds_write_b32 v1, a12 offset:3168
	ds_write_b32 v1, a13 offset:3300
	ds_write_b32 v1, a14 offset:3432
	ds_write_b32 v1, a15 offset:3564
	v_bfe_u32 v6, v0, 2, 5
	v_and_b32_e32 v7, 3, v0
	v_lshlrev_b32_e32 v9, 3, v7
	v_readfirstlane_b32 s30, v0
	v_sub_u32_e32 v10, v6, v9
	s_waitcnt lgkmcnt(0)
	s_barrier
	s_cmpk_ge_u32 s30, 0x80
	s_cbranch_scc1 .Llg_k1
	v_mul_u32_u24_e32 v2, 0x84, v6
	v_lshlrev_b32_e32 v8, 5, v7
	v_add_u32_e32 v2, v2, v8
	v_add_u32_e32 v8, 0x4280, v8
	v_add_u32_e32 v3, 0x1080, v2
	v_add_u32_e32 v4, 0x2100, v2
	v_add_u32_e32 v5, 0x3180, v2
	ds_read_b128 v[48:51], v8
	ds_read_b128 v[52:55], v8 offset:16
	ds_read2_b32 v[16:17], v2 offset0:0 offset1:1
	ds_read2_b32 v[18:19], v2 offset0:2 offset1:3
	ds_read2_b32 v[20:21], v2 offset0:4 offset1:5
	ds_read2_b32 v[22:23], v2 offset0:6 offset1:7
	ds_read2_b32 v[24:25], v3 offset0:0 offset1:1
	ds_read2_b32 v[26:27], v3 offset0:2 offset1:3
	ds_read2_b32 v[28:29], v3 offset0:4 offset1:5
	ds_read2_b32 v[30:31], v3 offset0:6 offset1:7
	ds_read2_b32 v[32:33], v4 offset0:0 offset1:1
	ds_read2_b32 v[34:35], v4 offset0:2 offset1:3
	ds_read2_b32 v[36:37], v4 offset0:4 offset1:5
	ds_read2_b32 v[38:39], v4 offset0:6 offset1:7
	s_waitcnt lgkmcnt(4)
	ds_read2_b32 v[40:41], v5 offset0:0 offset1:1
	ds_read2_b32 v[42:43], v5 offset0:2 offset1:3
	ds_read2_b32 v[44:45], v5 offset0:4 offset1:5
	ds_read2_b32 v[46:47], v5 offset0:6 offset1:7
	s_waitcnt lgkmcnt(0)
	s_branch .Llg_join
